# staggered epilogues in MoE gate/up and down GEMMs: per-unit epilogue-alignment barrier pair removed so one half's epilogue overlaps the other half's MFMA block
# baseline (speedup 1.0000x reference)
.LBB0_1657:
	s_and_b64 vcc, s[12:13], s[0:1]
	s_cbranch_vccz .LBB0_1659
	s_barrier
.LBB0_1659:
	s_mov_b32 s18, 0xbd38aa3b
	s_mov_b32 s20, 0x43000000
	v_lshl_add_u32 v6, s52, 8, v215
	v_readlane_b32 s4, v246, 11
	v_readlane_b32 s5, v246, 12
	v_ashrrev_i32_e32 v7, 31, v6
	v_lshl_or_b32 v4, s53, 7, v216
	v_lshlrev_b64 v[6:7], 10, v[6:7]
	v_ashrrev_i32_e32 v5, 31, v4
	v_lshl_add_u64 v[6:7], s[4:5], 0, v[6:7]
	v_lshl_add_u64 v[248:249], v[6:7], 0, v[4:5]
	v_mul_f32_e32 v2, s18, v190
	v_mul_f32_e32 v6, s18, v186
	v_mul_f32_e32 v3, s18, v191
	v_mul_f32_e32 v7, s18, v187
	v_mul_f32_e32 v4, s18, v192
	v_mul_f32_e32 v16, s18, v188
	v_mul_f32_e32 v5, s18, v193
	v_mul_f32_e32 v17, s18, v189
	v_exp_f32_e32 v2, v2
	v_exp_f32_e32 v6, v6
	v_exp_f32_e32 v3, v3
	v_exp_f32_e32 v7, v7
	v_exp_f32_e32 v4, v4
	v_exp_f32_e32 v16, v16
	v_exp_f32_e32 v5, v5
	v_exp_f32_e32 v17, v17
	v_pk_mul_f32 v[12:13], v[190:191], v[182:183]
	v_pk_mul_f32 v[14:15], v[192:193], v[184:185]
	v_pk_mul_f32 v[18:19], v[186:187], v[178:179]
	v_pk_mul_f32 v[20:21], v[188:189], v[180:181]
	v_fma_f32 v2, v2, s20, s20
	v_fma_f32 v6, v6, s20, s20
	v_fma_f32 v3, v3, s20, s20
	v_fma_f32 v7, v7, s20, s20
	v_fma_f32 v4, v4, s20, s20
	v_fma_f32 v16, v16, s20, s20
	v_fma_f32 v5, v5, s20, s20
	v_fma_f32 v17, v17, s20, s20
	v_rcp_f32_e32 v2, v2
	v_rcp_f32_e32 v6, v6
	v_rcp_f32_e32 v3, v3
	v_rcp_f32_e32 v7, v7
	v_rcp_f32_e32 v4, v4
	v_rcp_f32_e32 v16, v16
	v_rcp_f32_e32 v5, v5
	v_rcp_f32_e32 v17, v17
	v_pk_mul_f32 v[12:13], v[12:13], v[2:3]
	v_pk_mul_f32 v[18:19], v[18:19], v[6:7]
	v_pk_mul_f32 v[14:15], v[14:15], v[4:5]
	v_pk_mul_f32 v[20:21], v[20:21], v[16:17]
	v_med3_f32 v12, v12, s46, v204
	v_med3_f32 v18, v18, s46, v204
	v_med3_f32 v13, v13, s46, v204
	v_med3_f32 v19, v19, s46, v204
	v_med3_f32 v14, v14, s46, v204
	v_med3_f32 v20, v20, s46, v204
	v_med3_f32 v15, v15, s46, v204
	v_med3_f32 v21, v21, s46, v204
	v_cvt_pk_fp8_f32 v8, v12, v13
	v_cvt_pk_fp8_f32 v9, v18, v19
	v_cvt_pk_fp8_f32 v8, v14, v15 op_sel:[0,0,1]
	v_cvt_pk_fp8_f32 v9, v20, v21 op_sel:[0,0,1]
	v_mul_f32_e32 v2, s18, v174
	v_mul_f32_e32 v6, s18, v170
	v_mul_f32_e32 v3, s18, v175
	v_mul_f32_e32 v7, s18, v171
	v_mul_f32_e32 v4, s18, v176
	v_mul_f32_e32 v16, s18, v172
	v_mul_f32_e32 v5, s18, v177
	v_mul_f32_e32 v17, s18, v173
	v_exp_f32_e32 v2, v2
	v_exp_f32_e32 v6, v6
	v_exp_f32_e32 v3, v3
	v_exp_f32_e32 v7, v7
	v_exp_f32_e32 v4, v4
	v_exp_f32_e32 v16, v16
	v_exp_f32_e32 v5, v5
	v_exp_f32_e32 v17, v17
	v_pk_mul_f32 v[12:13], v[174:175], v[166:167]
	v_pk_mul_f32 v[14:15], v[176:177], v[168:169]
	v_pk_mul_f32 v[18:19], v[170:171], v[162:163]
	v_pk_mul_f32 v[20:21], v[172:173], v[164:165]
	v_fma_f32 v2, v2, s20, s20
	v_fma_f32 v6, v6, s20, s20
	v_fma_f32 v3, v3, s20, s20
	v_fma_f32 v7, v7, s20, s20
	v_fma_f32 v4, v4, s20, s20
	v_fma_f32 v16, v16, s20, s20
	v_fma_f32 v5, v5, s20, s20
	v_fma_f32 v17, v17, s20, s20
	v_rcp_f32_e32 v2, v2
	v_rcp_f32_e32 v6, v6
	v_rcp_f32_e32 v3, v3
	v_rcp_f32_e32 v7, v7
	v_rcp_f32_e32 v4, v4
	v_rcp_f32_e32 v16, v16
	v_rcp_f32_e32 v5, v5
	v_rcp_f32_e32 v17, v17
	v_pk_mul_f32 v[12:13], v[12:13], v[2:3]
	v_pk_mul_f32 v[18:19], v[18:19], v[6:7]
	v_pk_mul_f32 v[14:15], v[14:15], v[4:5]
	v_pk_mul_f32 v[20:21], v[20:21], v[16:17]
	v_med3_f32 v12, v12, s46, v204
	v_med3_f32 v18, v18, s46, v204
	v_med3_f32 v13, v13, s46, v204
	v_med3_f32 v19, v19, s46, v204
	v_med3_f32 v14, v14, s46, v204
	v_med3_f32 v20, v20, s46, v204
	v_med3_f32 v15, v15, s46, v204
	v_med3_f32 v21, v21, s46, v204
	v_cvt_pk_fp8_f32 v10, v12, v13
	v_cvt_pk_fp8_f32 v11, v18, v19
	v_cvt_pk_fp8_f32 v10, v14, v15 op_sel:[0,0,1]
	v_cvt_pk_fp8_f32 v11, v20, v21 op_sel:[0,0,1]
	v_mov_b32_e32 v250, v248
	v_mov_b32_e32 v251, v249
	v_permlane16_swap_b32_e32 v8, v10
	v_permlane16_swap_b32_e32 v9, v11
	global_store_dwordx4 v[250:251], v[8:11], off
	v_mul_f32_e32 v2, s18, v158
	v_mul_f32_e32 v6, s18, v154
	v_mul_f32_e32 v3, s18, v159
	v_mul_f32_e32 v7, s18, v155
	v_mul_f32_e32 v4, s18, v160
	v_mul_f32_e32 v16, s18, v156
	v_mul_f32_e32 v5, s18, v161
	v_mul_f32_e32 v17, s18, v157
	v_exp_f32_e32 v2, v2
	v_exp_f32_e32 v6, v6
	v_exp_f32_e32 v3, v3
	v_exp_f32_e32 v7, v7
	v_exp_f32_e32 v4, v4
	v_exp_f32_e32 v16, v16
	v_exp_f32_e32 v5, v5
	v_exp_f32_e32 v17, v17
	v_pk_mul_f32 v[12:13], v[158:159], v[150:151]
	v_pk_mul_f32 v[14:15], v[160:161], v[152:153]
	v_pk_mul_f32 v[18:19], v[154:155], v[146:147]
	v_pk_mul_f32 v[20:21], v[156:157], v[148:149]
	v_fma_f32 v2, v2, s20, s20
	v_fma_f32 v6, v6, s20, s20
	v_fma_f32 v3, v3, s20, s20
	v_fma_f32 v7, v7, s20, s20
	v_fma_f32 v4, v4, s20, s20
	v_fma_f32 v16, v16, s20, s20
	v_fma_f32 v5, v5, s20, s20
	v_fma_f32 v17, v17, s20, s20
	v_rcp_f32_e32 v2, v2
	v_rcp_f32_e32 v6, v6
	v_rcp_f32_e32 v3, v3
	v_rcp_f32_e32 v7, v7
	v_rcp_f32_e32 v4, v4
	v_rcp_f32_e32 v16, v16
	v_rcp_f32_e32 v5, v5
	v_rcp_f32_e32 v17, v17
	v_pk_mul_f32 v[12:13], v[12:13], v[2:3]
	v_pk_mul_f32 v[18:19], v[18:19], v[6:7]
	v_pk_mul_f32 v[14:15], v[14:15], v[4:5]
	v_pk_mul_f32 v[20:21], v[20:21], v[16:17]
	v_med3_f32 v12, v12, s46, v204
	v_med3_f32 v18, v18, s46, v204
	v_med3_f32 v13, v13, s46, v204
	v_med3_f32 v19, v19, s46, v204
	v_med3_f32 v14, v14, s46, v204
	v_med3_f32 v20, v20, s46, v204
	v_med3_f32 v15, v15, s46, v204
	v_med3_f32 v21, v21, s46, v204
	v_cvt_pk_fp8_f32 v8, v12, v13
	v_cvt_pk_fp8_f32 v9, v18, v19
	v_cvt_pk_fp8_f32 v8, v14, v15 op_sel:[0,0,1]
	v_cvt_pk_fp8_f32 v9, v20, v21 op_sel:[0,0,1]
	v_mul_f32_e32 v2, s18, v142
	v_mul_f32_e32 v6, s18, v138
	v_mul_f32_e32 v3, s18, v143
	v_mul_f32_e32 v7, s18, v139
	v_mul_f32_e32 v4, s18, v144
	v_mul_f32_e32 v16, s18, v140
	v_mul_f32_e32 v5, s18, v145
	v_mul_f32_e32 v17, s18, v141
	v_exp_f32_e32 v2, v2
	v_exp_f32_e32 v6, v6
	v_exp_f32_e32 v3, v3
	v_exp_f32_e32 v7, v7
	v_exp_f32_e32 v4, v4
	v_exp_f32_e32 v16, v16
	v_exp_f32_e32 v5, v5
	v_exp_f32_e32 v17, v17
	v_pk_mul_f32 v[12:13], v[142:143], v[134:135]
	v_pk_mul_f32 v[14:15], v[144:145], v[136:137]
	v_pk_mul_f32 v[18:19], v[138:139], v[130:131]
	v_pk_mul_f32 v[20:21], v[140:141], v[132:133]
	v_fma_f32 v2, v2, s20, s20
	v_fma_f32 v6, v6, s20, s20
	v_fma_f32 v3, v3, s20, s20
	v_fma_f32 v7, v7, s20, s20
	v_fma_f32 v4, v4, s20, s20
	v_fma_f32 v16, v16, s20, s20
	v_fma_f32 v5, v5, s20, s20
	v_fma_f32 v17, v17, s20, s20
	v_rcp_f32_e32 v2, v2
	v_rcp_f32_e32 v6, v6
	v_rcp_f32_e32 v3, v3
	v_rcp_f32_e32 v7, v7
	v_rcp_f32_e32 v4, v4
	v_rcp_f32_e32 v16, v16
	v_rcp_f32_e32 v5, v5
	v_rcp_f32_e32 v17, v17
	v_pk_mul_f32 v[12:13], v[12:13], v[2:3]
	v_pk_mul_f32 v[18:19], v[18:19], v[6:7]
	v_pk_mul_f32 v[14:15], v[14:15], v[4:5]
	v_pk_mul_f32 v[20:21], v[20:21], v[16:17]
	v_med3_f32 v12, v12, s46, v204
	v_med3_f32 v18, v18, s46, v204
	v_med3_f32 v13, v13, s46, v204
	v_med3_f32 v19, v19, s46, v204
	v_med3_f32 v14, v14, s46, v204
	v_med3_f32 v20, v20, s46, v204
	v_med3_f32 v15, v15, s46, v204
	v_med3_f32 v21, v21, s46, v204
	v_cvt_pk_fp8_f32 v10, v12, v13
	v_cvt_pk_fp8_f32 v11, v18, v19
	v_cvt_pk_fp8_f32 v10, v14, v15 op_sel:[0,0,1]
	v_cvt_pk_fp8_f32 v11, v20, v21 op_sel:[0,0,1]
	s_mov_b64 s[4:5], 0x8000
	v_lshl_add_u64 v[250:251], v[248:249], 0, s[4:5]
	s_nop 0
	v_permlane16_swap_b32_e32 v8, v10
	v_permlane16_swap_b32_e32 v9, v11
	global_store_dwordx4 v[250:251], v[8:11], off
	v_mul_f32_e32 v2, s18, v126
	v_mul_f32_e32 v6, s18, v122
	v_mul_f32_e32 v3, s18, v127
	v_mul_f32_e32 v7, s18, v123
	v_mul_f32_e32 v4, s18, v128
	v_mul_f32_e32 v16, s18, v124
	v_mul_f32_e32 v5, s18, v129
	v_mul_f32_e32 v17, s18, v125
	v_exp_f32_e32 v2, v2
	v_exp_f32_e32 v6, v6
	v_exp_f32_e32 v3, v3
	v_exp_f32_e32 v7, v7
	v_exp_f32_e32 v4, v4
	v_exp_f32_e32 v16, v16
	v_exp_f32_e32 v5, v5
	v_exp_f32_e32 v17, v17
	v_pk_mul_f32 v[12:13], v[126:127], v[118:119]
	v_pk_mul_f32 v[14:15], v[128:129], v[120:121]
	v_pk_mul_f32 v[18:19], v[122:123], v[114:115]
	v_pk_mul_f32 v[20:21], v[124:125], v[116:117]
	v_fma_f32 v2, v2, s20, s20
	v_fma_f32 v6, v6, s20, s20
	v_fma_f32 v3, v3, s20, s20
	v_fma_f32 v7, v7, s20, s20
	v_fma_f32 v4, v4, s20, s20
	v_fma_f32 v16, v16, s20, s20
	v_fma_f32 v5, v5, s20, s20
	v_fma_f32 v17, v17, s20, s20
	v_rcp_f32_e32 v2, v2
	v_rcp_f32_e32 v6, v6
	v_rcp_f32_e32 v3, v3
	v_rcp_f32_e32 v7, v7
	v_rcp_f32_e32 v4, v4
	v_rcp_f32_e32 v16, v16
	v_rcp_f32_e32 v5, v5
	v_rcp_f32_e32 v17, v17
	v_pk_mul_f32 v[12:13], v[12:13], v[2:3]
	v_pk_mul_f32 v[18:19], v[18:19], v[6:7]
	v_pk_mul_f32 v[14:15], v[14:15], v[4:5]
	v_pk_mul_f32 v[20:21], v[20:21], v[16:17]
	v_med3_f32 v12, v12, s46, v204
	v_med3_f32 v18, v18, s46, v204
	v_med3_f32 v13, v13, s46, v204
	v_med3_f32 v19, v19, s46, v204
	v_med3_f32 v14, v14, s46, v204
	v_med3_f32 v20, v20, s46, v204
	v_med3_f32 v15, v15, s46, v204
	v_med3_f32 v21, v21, s46, v204
	v_cvt_pk_fp8_f32 v8, v12, v13
	v_cvt_pk_fp8_f32 v9, v18, v19
	v_cvt_pk_fp8_f32 v8, v14, v15 op_sel:[0,0,1]
	v_cvt_pk_fp8_f32 v9, v20, v21 op_sel:[0,0,1]
	v_mul_f32_e32 v2, s18, v110
	v_mul_f32_e32 v6, s18, v106
	v_mul_f32_e32 v3, s18, v111
	v_mul_f32_e32 v7, s18, v107
	v_mul_f32_e32 v4, s18, v112
	v_mul_f32_e32 v16, s18, v108
	v_mul_f32_e32 v5, s18, v113
	v_mul_f32_e32 v17, s18, v109
	v_exp_f32_e32 v2, v2
	v_exp_f32_e32 v6, v6
	v_exp_f32_e32 v3, v3
	v_exp_f32_e32 v7, v7
	v_exp_f32_e32 v4, v4
	v_exp_f32_e32 v16, v16
	v_exp_f32_e32 v5, v5
	v_exp_f32_e32 v17, v17
	v_pk_mul_f32 v[12:13], v[110:111], v[102:103]
	v_pk_mul_f32 v[14:15], v[112:113], v[104:105]
	v_pk_mul_f32 v[18:19], v[106:107], v[90:91]
	v_pk_mul_f32 v[20:21], v[108:109], v[92:93]
	v_fma_f32 v2, v2, s20, s20
	v_fma_f32 v6, v6, s20, s20
	v_fma_f32 v3, v3, s20, s20
	v_fma_f32 v7, v7, s20, s20
	v_fma_f32 v4, v4, s20, s20
	v_fma_f32 v16, v16, s20, s20
	v_fma_f32 v5, v5, s20, s20
	v_fma_f32 v17, v17, s20, s20
	v_rcp_f32_e32 v2, v2
	v_rcp_f32_e32 v6, v6
	v_rcp_f32_e32 v3, v3
	v_rcp_f32_e32 v7, v7
	v_rcp_f32_e32 v4, v4
	v_rcp_f32_e32 v16, v16
	v_rcp_f32_e32 v5, v5
	v_rcp_f32_e32 v17, v17
	v_pk_mul_f32 v[12:13], v[12:13], v[2:3]
	v_pk_mul_f32 v[18:19], v[18:19], v[6:7]
	v_pk_mul_f32 v[14:15], v[14:15], v[4:5]
	v_pk_mul_f32 v[20:21], v[20:21], v[16:17]
	v_med3_f32 v12, v12, s46, v204
	v_med3_f32 v18, v18, s46, v204
	v_med3_f32 v13, v13, s46, v204
	v_med3_f32 v19, v19, s46, v204
	v_med3_f32 v14, v14, s46, v204
	v_med3_f32 v20, v20, s46, v204
	v_med3_f32 v15, v15, s46, v204
	v_med3_f32 v21, v21, s46, v204
	v_cvt_pk_fp8_f32 v10, v12, v13
	v_cvt_pk_fp8_f32 v11, v18, v19
	v_cvt_pk_fp8_f32 v10, v14, v15 op_sel:[0,0,1]
	v_cvt_pk_fp8_f32 v11, v20, v21 op_sel:[0,0,1]
	s_mov_b64 s[4:5], 0x20000
	v_lshl_add_u64 v[250:251], v[248:249], 0, s[4:5]
	s_nop 0
	v_permlane16_swap_b32_e32 v8, v10
	v_permlane16_swap_b32_e32 v9, v11
	global_store_dwordx4 v[250:251], v[8:11], off
	v_mul_f32_e32 v2, s18, v86
	v_mul_f32_e32 v6, s18, v82
	v_mul_f32_e32 v3, s18, v87
	v_mul_f32_e32 v7, s18, v83
	v_mul_f32_e32 v4, s18, v88
	v_mul_f32_e32 v16, s18, v84
	v_mul_f32_e32 v5, s18, v89
	v_mul_f32_e32 v17, s18, v85
	v_exp_f32_e32 v2, v2
	v_exp_f32_e32 v6, v6
	v_exp_f32_e32 v3, v3
	v_exp_f32_e32 v7, v7
	v_exp_f32_e32 v4, v4
	v_exp_f32_e32 v16, v16
	v_exp_f32_e32 v5, v5
	v_exp_f32_e32 v17, v17
	v_pk_mul_f32 v[12:13], v[86:87], v[98:99]
	v_pk_mul_f32 v[14:15], v[88:89], v[100:101]
	v_pk_mul_f32 v[18:19], v[82:83], v[94:95]
	v_pk_mul_f32 v[20:21], v[84:85], v[96:97]
	v_fma_f32 v2, v2, s20, s20
	v_fma_f32 v6, v6, s20, s20
	v_fma_f32 v3, v3, s20, s20
	v_fma_f32 v7, v7, s20, s20
	v_fma_f32 v4, v4, s20, s20
	v_fma_f32 v16, v16, s20, s20
	v_fma_f32 v5, v5, s20, s20
	v_fma_f32 v17, v17, s20, s20
	v_rcp_f32_e32 v2, v2
	v_rcp_f32_e32 v6, v6
	v_rcp_f32_e32 v3, v3
	v_rcp_f32_e32 v7, v7
	v_rcp_f32_e32 v4, v4
	v_rcp_f32_e32 v16, v16
	v_rcp_f32_e32 v5, v5
	v_rcp_f32_e32 v17, v17
	v_pk_mul_f32 v[12:13], v[12:13], v[2:3]
	v_pk_mul_f32 v[18:19], v[18:19], v[6:7]
	v_pk_mul_f32 v[14:15], v[14:15], v[4:5]
	v_pk_mul_f32 v[20:21], v[20:21], v[16:17]
	v_med3_f32 v12, v12, s46, v204
	v_med3_f32 v18, v18, s46, v204
	v_med3_f32 v13, v13, s46, v204
	v_med3_f32 v19, v19, s46, v204
	v_med3_f32 v14, v14, s46, v204
	v_med3_f32 v20, v20, s46, v204
	v_med3_f32 v15, v15, s46, v204
	v_med3_f32 v21, v21, s46, v204
	v_cvt_pk_fp8_f32 v8, v12, v13
	v_cvt_pk_fp8_f32 v9, v18, v19
	v_cvt_pk_fp8_f32 v8, v14, v15 op_sel:[0,0,1]
	v_cvt_pk_fp8_f32 v9, v20, v21 op_sel:[0,0,1]
	v_mul_f32_e32 v2, s18, v70
	v_mul_f32_e32 v6, s18, v66
	v_mul_f32_e32 v3, s18, v71
	v_mul_f32_e32 v7, s18, v67
	v_mul_f32_e32 v4, s18, v72
	v_mul_f32_e32 v16, s18, v68
	v_mul_f32_e32 v5, s18, v73
	v_mul_f32_e32 v17, s18, v69
	v_exp_f32_e32 v2, v2
	v_exp_f32_e32 v6, v6
	v_exp_f32_e32 v3, v3
	v_exp_f32_e32 v7, v7
	v_exp_f32_e32 v4, v4
	v_exp_f32_e32 v16, v16
	v_exp_f32_e32 v5, v5
	v_exp_f32_e32 v17, v17
	v_pk_mul_f32 v[12:13], v[70:71], v[78:79]
	v_pk_mul_f32 v[14:15], v[72:73], v[80:81]
	v_pk_mul_f32 v[18:19], v[66:67], v[74:75]
	v_pk_mul_f32 v[20:21], v[68:69], v[76:77]
	v_fma_f32 v2, v2, s20, s20
	v_fma_f32 v6, v6, s20, s20
	v_fma_f32 v3, v3, s20, s20
	v_fma_f32 v7, v7, s20, s20
	v_fma_f32 v4, v4, s20, s20
	v_fma_f32 v16, v16, s20, s20
	v_fma_f32 v5, v5, s20, s20
	v_fma_f32 v17, v17, s20, s20
	v_rcp_f32_e32 v2, v2
	v_rcp_f32_e32 v6, v6
	v_rcp_f32_e32 v3, v3
	v_rcp_f32_e32 v7, v7
	v_rcp_f32_e32 v4, v4
	v_rcp_f32_e32 v16, v16
	v_rcp_f32_e32 v5, v5
	v_rcp_f32_e32 v17, v17
	v_pk_mul_f32 v[12:13], v[12:13], v[2:3]
	v_pk_mul_f32 v[18:19], v[18:19], v[6:7]
	v_pk_mul_f32 v[14:15], v[14:15], v[4:5]
	v_pk_mul_f32 v[20:21], v[20:21], v[16:17]
	v_med3_f32 v12, v12, s46, v204
	v_med3_f32 v18, v18, s46, v204
	v_med3_f32 v13, v13, s46, v204
	v_med3_f32 v19, v19, s46, v204
	v_med3_f32 v14, v14, s46, v204
	v_med3_f32 v20, v20, s46, v204
	v_med3_f32 v15, v15, s46, v204
	v_med3_f32 v21, v21, s46, v204
	v_cvt_pk_fp8_f32 v10, v12, v13
	v_cvt_pk_fp8_f32 v11, v18, v19
	v_cvt_pk_fp8_f32 v10, v14, v15 op_sel:[0,0,1]
	v_cvt_pk_fp8_f32 v11, v20, v21 op_sel:[0,0,1]
	s_mov_b64 s[4:5], 0x28000
	v_lshl_add_u64 v[250:251], v[248:249], 0, s[4:5]
	s_nop 0
	v_permlane16_swap_b32_e32 v8, v10
	v_permlane16_swap_b32_e32 v9, v11
	s_and_b64 vcc, exec, s[0:1]
	s_mov_b64 s[0:1], -1
	global_store_dwordx4 v[250:251], v[8:11], off
	s_cbranch_vccnz .LBB0_1638
	s_branch .LBB0_1637

.LBB0_1814:
	s_mov_b32 s4, 0x3d000000
	v_pk_mul_f32 v[14:15], v[192:193], s[4:5] op_sel_hi:[1,0]
	v_pk_mul_f32 v[16:17], v[190:191], s[4:5] op_sel_hi:[1,0]
	v_pk_mul_f32 v[24:25], v[186:187], s[4:5] op_sel_hi:[1,0]
	v_med3_f32 v16, v16, s46, v204
	v_med3_f32 v17, v17, s46, v204
	v_med3_f32 v26, v14, s46, v204
	v_mov_b32_e32 v14, v195
	v_med3_f32 v27, v15, s46, v204
	v_cvt_pk_fp8_f32 v14, v16, v17
	v_med3_f32 v16, v24, s46, v204
	v_med3_f32 v17, v25, s46, v204
	v_mov_b32_e32 v15, v195
	v_cvt_pk_fp8_f32 v15, v16, v17
	s_nop 15
	s_nop 15
	v_lshl_add_u32 v6, s52, 10, v215
	v_pk_mul_f32 v[22:23], v[188:189], s[4:5] op_sel_hi:[1,0]
	ds_read2_b32 v[2:3], v6 offset1:16
	ds_read2_b32 v[4:5], v6 offset0:32 offset1:48
	v_med3_f32 v16, v22, s46, v204
	v_med3_f32 v17, v23, s46, v204
	v_cvt_pk_fp8_f32 v15, v16, v17 op_sel:[0,0,1]
	v_pk_mul_f32 v[16:17], v[184:185], s[4:5] op_sel_hi:[1,0]
	v_pk_mul_f32 v[22:23], v[182:183], s[4:5] op_sel_hi:[1,0]
	v_cvt_pk_fp8_f32 v14, v26, v27 op_sel:[0,0,1]
	v_pk_mul_f32 v[26:27], v[178:179], s[4:5] op_sel_hi:[1,0]
	v_med3_f32 v22, v22, s46, v204
	v_med3_f32 v23, v23, s46, v204
	v_med3_f32 v28, v16, s46, v204
	v_mov_b32_e32 v16, v195
	v_med3_f32 v29, v17, s46, v204
	v_cvt_pk_fp8_f32 v16, v22, v23
	v_med3_f32 v22, v26, s46, v204
	v_med3_f32 v23, v27, s46, v204
	v_mov_b32_e32 v17, v195
	v_cvt_pk_fp8_f32 v17, v22, v23
	s_waitcnt lgkmcnt(0)
	v_mov_b32_e32 v20, v4
	v_mov_b32_e32 v12, v5
	ds_read2_b32 v[4:5], v6 offset0:160 offset1:176
	v_mov_b32_e32 v194, v2
	v_mov_b32_e32 v18, v3
	ds_read2_b32 v[2:3], v6 offset0:128 offset1:144
	v_pk_mul_f32 v[24:25], v[180:181], s[4:5] op_sel_hi:[1,0]
	v_cvt_pk_fp8_f32 v16, v28, v29 op_sel:[0,0,1]
	v_med3_f32 v22, v24, s46, v204
	v_med3_f32 v23, v25, s46, v204
	v_cvt_pk_fp8_f32 v17, v22, v23 op_sel:[0,0,1]
	s_waitcnt lgkmcnt(1)
	v_mov_b32_e32 v6, v4
	v_lshl_or_b32 v4, s51, 8, v216
	s_waitcnt lgkmcnt(0)
	v_mov_b32_e32 v10, v2
	v_mov_b32_e32 v2, v5
	v_ashrrev_i32_e32 v5, 31, v4
	v_lshl_add_u64 v[22:23], s[56:57], 0, v[194:195]
	v_permlane16_swap_b32_e32 v14, v16
	v_permlane16_swap_b32_e32 v15, v17
	v_lshl_add_u64 v[22:23], v[22:23], 0, v[4:5]
	global_store_dwordx4 v[22:23], v[14:17], off
	v_pk_mul_f32 v[24:25], v[170:171], s[4:5] op_sel_hi:[1,0]
	v_pk_mul_f32 v[22:23], v[172:173], s[4:5] op_sel_hi:[1,0]
	v_pk_mul_f32 v[14:15], v[176:177], s[4:5] op_sel_hi:[1,0]
	v_pk_mul_f32 v[16:17], v[174:175], s[4:5] op_sel_hi:[1,0]
	v_med3_f32 v26, v14, s46, v204
	v_med3_f32 v16, v16, s46, v204
	v_med3_f32 v17, v17, s46, v204
	v_mov_b32_e32 v14, v195
	v_med3_f32 v27, v15, s46, v204
	v_cvt_pk_fp8_f32 v14, v16, v17
	v_med3_f32 v16, v24, s46, v204
	v_med3_f32 v17, v25, s46, v204
	v_mov_b32_e32 v15, v195
	v_cvt_pk_fp8_f32 v15, v16, v17
	v_med3_f32 v16, v22, s46, v204
	v_med3_f32 v17, v23, s46, v204
	v_pk_mul_f32 v[22:23], v[166:167], s[4:5] op_sel_hi:[1,0]
	v_cvt_pk_fp8_f32 v15, v16, v17 op_sel:[0,0,1]
	v_pk_mul_f32 v[16:17], v[168:169], s[4:5] op_sel_hi:[1,0]
	v_cvt_pk_fp8_f32 v14, v26, v27 op_sel:[0,0,1]
	v_pk_mul_f32 v[26:27], v[162:163], s[4:5] op_sel_hi:[1,0]
	v_med3_f32 v22, v22, s46, v204
	v_med3_f32 v23, v23, s46, v204
	v_med3_f32 v28, v16, s46, v204
	v_mov_b32_e32 v16, v195
	v_med3_f32 v29, v17, s46, v204
	v_cvt_pk_fp8_f32 v16, v22, v23
	v_med3_f32 v22, v26, s46, v204
	v_med3_f32 v23, v27, s46, v204
	v_mov_b32_e32 v17, v195
	v_cvt_pk_fp8_f32 v17, v22, v23
	v_pk_mul_f32 v[24:25], v[164:165], s[4:5] op_sel_hi:[1,0]
	v_cvt_pk_fp8_f32 v16, v28, v29 op_sel:[0,0,1]
	v_med3_f32 v22, v24, s46, v204
	v_med3_f32 v23, v25, s46, v204
	v_cvt_pk_fp8_f32 v17, v22, v23 op_sel:[0,0,1]
	v_mov_b32_e32 v19, v195
	v_lshl_add_u64 v[18:19], s[56:57], 0, v[18:19]
	v_permlane16_swap_b32_e32 v14, v16
	v_permlane16_swap_b32_e32 v15, v17
	v_lshl_add_u64 v[18:19], v[18:19], 0, v[4:5]
	global_store_dwordx4 v[18:19], v[14:17], off
	v_pk_mul_f32 v[22:23], v[154:155], s[4:5] op_sel_hi:[1,0]
	v_pk_mul_f32 v[18:19], v[156:157], s[4:5] op_sel_hi:[1,0]
	v_pk_mul_f32 v[14:15], v[160:161], s[4:5] op_sel_hi:[1,0]
	v_pk_mul_f32 v[16:17], v[158:159], s[4:5] op_sel_hi:[1,0]
	v_med3_f32 v24, v14, s46, v204
	v_med3_f32 v16, v16, s46, v204
	v_med3_f32 v17, v17, s46, v204
	v_mov_b32_e32 v14, v195
	v_med3_f32 v25, v15, s46, v204
	v_cvt_pk_fp8_f32 v14, v16, v17
	v_med3_f32 v16, v22, s46, v204
	v_med3_f32 v17, v23, s46, v204
	v_mov_b32_e32 v15, v195
	v_cvt_pk_fp8_f32 v15, v16, v17
	v_med3_f32 v16, v18, s46, v204
	v_med3_f32 v17, v19, s46, v204
	v_pk_mul_f32 v[18:19], v[150:151], s[4:5] op_sel_hi:[1,0]
	v_cvt_pk_fp8_f32 v15, v16, v17 op_sel:[0,0,1]
	v_pk_mul_f32 v[16:17], v[152:153], s[4:5] op_sel_hi:[1,0]
	v_cvt_pk_fp8_f32 v14, v24, v25 op_sel:[0,0,1]
	v_pk_mul_f32 v[24:25], v[146:147], s[4:5] op_sel_hi:[1,0]
	v_med3_f32 v18, v18, s46, v204
	v_med3_f32 v19, v19, s46, v204
	v_med3_f32 v26, v16, s46, v204
	v_mov_b32_e32 v16, v195
	v_med3_f32 v27, v17, s46, v204
	v_cvt_pk_fp8_f32 v16, v18, v19
	v_med3_f32 v18, v24, s46, v204
	v_med3_f32 v19, v25, s46, v204
	v_mov_b32_e32 v17, v195
	v_cvt_pk_fp8_f32 v17, v18, v19
	v_pk_mul_f32 v[22:23], v[148:149], s[4:5] op_sel_hi:[1,0]
	v_cvt_pk_fp8_f32 v16, v26, v27 op_sel:[0,0,1]
	v_med3_f32 v18, v22, s46, v204
	v_med3_f32 v19, v23, s46, v204
	v_cvt_pk_fp8_f32 v17, v18, v19 op_sel:[0,0,1]
	v_mov_b32_e32 v21, v195
	v_lshl_add_u64 v[18:19], s[56:57], 0, v[20:21]
	v_permlane16_swap_b32_e32 v14, v16
	v_permlane16_swap_b32_e32 v15, v17
	v_lshl_add_u64 v[18:19], v[18:19], 0, v[4:5]
	global_store_dwordx4 v[18:19], v[14:17], off
	v_pk_mul_f32 v[20:21], v[138:139], s[4:5] op_sel_hi:[1,0]
	v_pk_mul_f32 v[18:19], v[140:141], s[4:5] op_sel_hi:[1,0]
	v_pk_mul_f32 v[14:15], v[144:145], s[4:5] op_sel_hi:[1,0]
	v_pk_mul_f32 v[16:17], v[142:143], s[4:5] op_sel_hi:[1,0]
	v_med3_f32 v22, v14, s46, v204
	v_med3_f32 v16, v16, s46, v204
	v_med3_f32 v17, v17, s46, v204
	v_mov_b32_e32 v14, v195
	v_med3_f32 v23, v15, s46, v204
	v_cvt_pk_fp8_f32 v14, v16, v17
	v_med3_f32 v16, v20, s46, v204
	v_med3_f32 v17, v21, s46, v204
	v_mov_b32_e32 v15, v195
	v_cvt_pk_fp8_f32 v15, v16, v17
	v_med3_f32 v16, v18, s46, v204
	v_med3_f32 v17, v19, s46, v204
	v_pk_mul_f32 v[18:19], v[134:135], s[4:5] op_sel_hi:[1,0]
	v_cvt_pk_fp8_f32 v15, v16, v17 op_sel:[0,0,1]
	v_pk_mul_f32 v[16:17], v[136:137], s[4:5] op_sel_hi:[1,0]
	v_cvt_pk_fp8_f32 v14, v22, v23 op_sel:[0,0,1]
	v_pk_mul_f32 v[22:23], v[130:131], s[4:5] op_sel_hi:[1,0]
	v_med3_f32 v18, v18, s46, v204
	v_med3_f32 v19, v19, s46, v204
	v_med3_f32 v24, v16, s46, v204
	v_mov_b32_e32 v16, v195
	v_med3_f32 v25, v17, s46, v204
	v_cvt_pk_fp8_f32 v16, v18, v19
	v_med3_f32 v18, v22, s46, v204
	v_med3_f32 v19, v23, s46, v204
	v_mov_b32_e32 v17, v195
	v_cvt_pk_fp8_f32 v17, v18, v19
	v_pk_mul_f32 v[20:21], v[132:133], s[4:5] op_sel_hi:[1,0]
	v_cvt_pk_fp8_f32 v16, v24, v25 op_sel:[0,0,1]
	v_med3_f32 v18, v20, s46, v204
	v_med3_f32 v19, v21, s46, v204
	v_cvt_pk_fp8_f32 v17, v18, v19 op_sel:[0,0,1]
	v_mov_b32_e32 v13, v195
	v_lshl_add_u64 v[12:13], s[56:57], 0, v[12:13]
	v_permlane16_swap_b32_e32 v14, v16
	v_permlane16_swap_b32_e32 v15, v17
	v_lshl_add_u64 v[12:13], v[12:13], 0, v[4:5]
	global_store_dwordx4 v[12:13], v[14:17], off
	v_pk_mul_f32 v[12:13], v[128:129], s[4:5] op_sel_hi:[1,0]
	v_pk_mul_f32 v[18:19], v[122:123], s[4:5] op_sel_hi:[1,0]
	v_pk_mul_f32 v[14:15], v[126:127], s[4:5] op_sel_hi:[1,0]
	v_med3_f32 v20, v12, s46, v204
	v_med3_f32 v14, v14, s46, v204
	v_med3_f32 v15, v15, s46, v204
	v_mov_b32_e32 v12, v195
	v_med3_f32 v21, v13, s46, v204
	v_cvt_pk_fp8_f32 v12, v14, v15
	v_med3_f32 v14, v18, s46, v204
	v_med3_f32 v15, v19, s46, v204
	v_mov_b32_e32 v13, v195
	v_cvt_pk_fp8_f32 v13, v14, v15
	v_pk_mul_f32 v[16:17], v[124:125], s[4:5] op_sel_hi:[1,0]
	v_cvt_pk_fp8_f32 v12, v20, v21 op_sel:[0,0,1]
	v_med3_f32 v14, v16, s46, v204
	v_med3_f32 v15, v17, s46, v204
	v_cvt_pk_fp8_f32 v13, v14, v15 op_sel:[0,0,1]
	v_pk_mul_f32 v[14:15], v[120:121], s[4:5] op_sel_hi:[1,0]
	v_pk_mul_f32 v[16:17], v[118:119], s[4:5] op_sel_hi:[1,0]
	v_pk_mul_f32 v[20:21], v[114:115], s[4:5] op_sel_hi:[1,0]
	v_med3_f32 v16, v16, s46, v204
	v_med3_f32 v17, v17, s46, v204
	v_med3_f32 v22, v14, s46, v204
	v_mov_b32_e32 v14, v195
	v_med3_f32 v23, v15, s46, v204
	v_cvt_pk_fp8_f32 v14, v16, v17
	v_med3_f32 v16, v20, s46, v204
	v_med3_f32 v17, v21, s46, v204
	v_mov_b32_e32 v15, v195
	v_cvt_pk_fp8_f32 v15, v16, v17
	v_pk_mul_f32 v[18:19], v[116:117], s[4:5] op_sel_hi:[1,0]
	v_cvt_pk_fp8_f32 v14, v22, v23 op_sel:[0,0,1]
	v_med3_f32 v16, v18, s46, v204
	v_med3_f32 v17, v19, s46, v204
	v_cvt_pk_fp8_f32 v15, v16, v17 op_sel:[0,0,1]
	v_mov_b32_e32 v11, v195
	v_lshl_add_u64 v[10:11], s[56:57], 0, v[10:11]
	v_permlane16_swap_b32_e32 v12, v14
	v_permlane16_swap_b32_e32 v13, v15
	v_lshl_add_u64 v[10:11], v[10:11], 0, v[4:5]
	global_store_dwordx4 v[10:11], v[12:15], off
	v_pk_mul_f32 v[10:11], v[112:113], s[4:5] op_sel_hi:[1,0]
	v_pk_mul_f32 v[16:17], v[106:107], s[4:5] op_sel_hi:[1,0]
	v_pk_mul_f32 v[12:13], v[110:111], s[4:5] op_sel_hi:[1,0]
	v_med3_f32 v18, v10, s46, v204
	v_med3_f32 v12, v12, s46, v204
	v_med3_f32 v13, v13, s46, v204
	v_mov_b32_e32 v10, v195
	v_med3_f32 v19, v11, s46, v204
	v_cvt_pk_fp8_f32 v10, v12, v13
	v_med3_f32 v12, v16, s46, v204
	v_med3_f32 v13, v17, s46, v204
	v_mov_b32_e32 v11, v195
	v_cvt_pk_fp8_f32 v11, v12, v13
	v_pk_mul_f32 v[14:15], v[108:109], s[4:5] op_sel_hi:[1,0]
	v_cvt_pk_fp8_f32 v10, v18, v19 op_sel:[0,0,1]
	v_med3_f32 v12, v14, s46, v204
	v_med3_f32 v13, v15, s46, v204
	v_cvt_pk_fp8_f32 v11, v12, v13 op_sel:[0,0,1]
	v_pk_mul_f32 v[12:13], v[96:97], s[4:5] op_sel_hi:[1,0]
	v_pk_mul_f32 v[14:15], v[94:95], s[4:5] op_sel_hi:[1,0]
	v_pk_mul_f32 v[18:19], v[90:91], s[4:5] op_sel_hi:[1,0]
	v_med3_f32 v14, v14, s46, v204
	v_med3_f32 v15, v15, s46, v204
	v_med3_f32 v20, v12, s46, v204
	v_mov_b32_e32 v12, v195
	v_med3_f32 v21, v13, s46, v204
	v_cvt_pk_fp8_f32 v12, v14, v15
	v_med3_f32 v14, v18, s46, v204
	v_med3_f32 v15, v19, s46, v204
	v_mov_b32_e32 v13, v195
	v_cvt_pk_fp8_f32 v13, v14, v15
	v_pk_mul_f32 v[16:17], v[92:93], s[4:5] op_sel_hi:[1,0]
	v_cvt_pk_fp8_f32 v12, v20, v21 op_sel:[0,0,1]
	v_med3_f32 v14, v16, s46, v204
	v_med3_f32 v15, v17, s46, v204
	v_cvt_pk_fp8_f32 v13, v14, v15 op_sel:[0,0,1]
	v_mov_b32_e32 v8, v3
	v_mov_b32_e32 v9, v195
	v_lshl_add_u64 v[8:9], s[56:57], 0, v[8:9]
	v_permlane16_swap_b32_e32 v10, v12
	v_permlane16_swap_b32_e32 v11, v13
	v_lshl_add_u64 v[8:9], v[8:9], 0, v[4:5]
	global_store_dwordx4 v[8:9], v[10:13], off
	v_pk_mul_f32 v[8:9], v[88:89], s[4:5] op_sel_hi:[1,0]
	v_pk_mul_f32 v[14:15], v[74:75], s[4:5] op_sel_hi:[1,0]
	v_pk_mul_f32 v[10:11], v[86:87], s[4:5] op_sel_hi:[1,0]
	v_med3_f32 v16, v8, s46, v204
	v_med3_f32 v10, v10, s46, v204
	v_med3_f32 v11, v11, s46, v204
	v_mov_b32_e32 v8, v195
	v_med3_f32 v17, v9, s46, v204
	v_cvt_pk_fp8_f32 v8, v10, v11
	v_med3_f32 v10, v14, s46, v204
	v_med3_f32 v11, v15, s46, v204
	v_mov_b32_e32 v9, v195
	v_cvt_pk_fp8_f32 v9, v10, v11
	v_pk_mul_f32 v[12:13], v[76:77], s[4:5] op_sel_hi:[1,0]
	v_cvt_pk_fp8_f32 v8, v16, v17 op_sel:[0,0,1]
	v_med3_f32 v10, v12, s46, v204
	v_med3_f32 v11, v13, s46, v204
	v_cvt_pk_fp8_f32 v9, v10, v11 op_sel:[0,0,1]
	v_pk_mul_f32 v[10:11], v[104:105], s[4:5] op_sel_hi:[1,0]
	v_pk_mul_f32 v[12:13], v[102:103], s[4:5] op_sel_hi:[1,0]
	v_pk_mul_f32 v[16:17], v[98:99], s[4:5] op_sel_hi:[1,0]
	v_med3_f32 v12, v12, s46, v204
	v_med3_f32 v13, v13, s46, v204
	v_med3_f32 v18, v10, s46, v204
	v_mov_b32_e32 v10, v195
	v_med3_f32 v19, v11, s46, v204
	v_cvt_pk_fp8_f32 v10, v12, v13
	v_med3_f32 v12, v16, s46, v204
	v_med3_f32 v13, v17, s46, v204
	v_mov_b32_e32 v11, v195
	v_cvt_pk_fp8_f32 v11, v12, v13
	v_pk_mul_f32 v[14:15], v[100:101], s[4:5] op_sel_hi:[1,0]
	v_cvt_pk_fp8_f32 v10, v18, v19 op_sel:[0,0,1]
	v_med3_f32 v12, v14, s46, v204
	v_med3_f32 v13, v15, s46, v204
	v_cvt_pk_fp8_f32 v11, v12, v13 op_sel:[0,0,1]
	v_mov_b32_e32 v7, v195
	v_lshl_add_u64 v[6:7], s[56:57], 0, v[6:7]
	v_permlane16_swap_b32_e32 v8, v10
	v_permlane16_swap_b32_e32 v9, v11
	v_lshl_add_u64 v[6:7], v[6:7], 0, v[4:5]
	global_store_dwordx4 v[6:7], v[8:11], off
	v_pk_mul_f32 v[6:7], v[72:73], s[4:5] op_sel_hi:[1,0]
	v_pk_mul_f32 v[12:13], v[66:67], s[4:5] op_sel_hi:[1,0]
	v_pk_mul_f32 v[8:9], v[70:71], s[4:5] op_sel_hi:[1,0]
	v_med3_f32 v14, v6, s46, v204
	v_med3_f32 v8, v8, s46, v204
	v_med3_f32 v9, v9, s46, v204
	v_mov_b32_e32 v6, v195
	v_med3_f32 v15, v7, s46, v204
	v_cvt_pk_fp8_f32 v6, v8, v9
	v_med3_f32 v8, v12, s46, v204
	v_med3_f32 v9, v13, s46, v204
	v_mov_b32_e32 v7, v195
	v_cvt_pk_fp8_f32 v7, v8, v9
	v_pk_mul_f32 v[10:11], v[68:69], s[4:5] op_sel_hi:[1,0]
	v_cvt_pk_fp8_f32 v6, v14, v15 op_sel:[0,0,1]
	v_med3_f32 v8, v10, s46, v204
	v_med3_f32 v9, v11, s46, v204
	v_cvt_pk_fp8_f32 v7, v8, v9 op_sel:[0,0,1]
	v_pk_mul_f32 v[8:9], v[84:85], s[4:5] op_sel_hi:[1,0]
	v_pk_mul_f32 v[10:11], v[82:83], s[4:5] op_sel_hi:[1,0]
	v_pk_mul_f32 v[14:15], v[78:79], s[4:5] op_sel_hi:[1,0]
	v_med3_f32 v10, v10, s46, v204
	v_med3_f32 v11, v11, s46, v204
	v_med3_f32 v16, v8, s46, v204
	v_mov_b32_e32 v8, v195
	v_med3_f32 v17, v9, s46, v204
	v_cvt_pk_fp8_f32 v8, v10, v11
	v_med3_f32 v10, v14, s46, v204
	v_med3_f32 v11, v15, s46, v204
	v_mov_b32_e32 v9, v195
	v_cvt_pk_fp8_f32 v9, v10, v11
	v_pk_mul_f32 v[12:13], v[80:81], s[4:5] op_sel_hi:[1,0]
	v_cvt_pk_fp8_f32 v8, v16, v17 op_sel:[0,0,1]
	v_med3_f32 v10, v12, s46, v204
	v_med3_f32 v11, v13, s46, v204
	v_cvt_pk_fp8_f32 v9, v10, v11 op_sel:[0,0,1]
	v_mov_b32_e32 v3, v195
	v_lshl_add_u64 v[2:3], s[56:57], 0, v[2:3]
	v_permlane16_swap_b32_e32 v6, v8
	v_permlane16_swap_b32_e32 v7, v9
	v_lshl_add_u64 v[2:3], v[2:3], 0, v[4:5]
	s_and_b64 vcc, exec, s[0:1]
	s_mov_b64 s[0:1], -1
	global_store_dwordx4 v[2:3], v[6:9], off
	s_cbranch_vccnz .LBB0_1793
	s_branch .LBB0_1792
